# v51 plus second poll bank issued s_sleep 3 later (evenly spaced samples between the two banks)
# speedup vs baseline: 1.0188x; 1.0016x over previous
.Lr0_rdy:
	v_lshl_add_u32 v66, s54, 11, v1
	ds_read_b128 a[0:3], v66
	ds_read_b128 a[4:7], v66 offset:1024
	s_cmp_eq_u32 s54, 0
	s_cbranch_scc1 .Lr0_first
	s_sleep 3
	global_load_dwordx4 v[164:167], v[196:197], off nt
	global_load_dwordx4 v[168:171], v[196:197], off offset:1024 nt
	global_load_dwordx4 v[172:175], v[196:197], off offset:2048 nt
	global_load_dwordx4 v[176:179], v[196:197], off offset:3072 nt
	global_load_dwordx4 v[180:183], v[198:199], off nt
	global_load_dwordx4 v[184:187], v[198:199], off offset:1024 nt
	global_load_dwordx4 v[188:191], v[198:199], off offset:2048 nt
	global_load_dwordx4 v[192:195], v[198:199], off offset:3072 nt
	s_mov_b32 s55, 0
	s_waitcnt lgkmcnt(0)
